# baseline (speedup 1.0000x reference)
_Z12chain_kernelILi0EEv9ChainArgs:
	s_load_dwordx16 s[4:19], s[0:1], 0x0
	v_lshrrev_b32_e32 v121, 6, v0
	v_and_b32_e32 v145, 63, v0
	v_mul_u32_u24_e32 v1, 0x900, v121
	v_or_b32_e32 v1, v1, v145
	v_mul_u32_u24_e32 v120, 0x556, v0
	v_mov_b32_e32 v94, 48
	s_bfe_i32 s3, s2, 0x10003
	v_lshlrev_b32_e32 v2, 4, v1
	v_mul_lo_u16_sdwa v1, v120, v94 dst_sel:DWORD dst_unused:UNUSED_PAD src0_sel:WORD_1 src1_sel:DWORD
	s_lshl_b32 s28, s2, 5
	s_and_b32 s3, s3, 0x1800
	v_sub_u16_e32 v1, v0, v1
	s_waitcnt lgkmcnt(0)
	s_add_u32 s20, s10, s3
	v_lshlrev_b16_e32 v124, 3, v1
	v_or_b32_e32 v1, 0x200, v0
	s_addc_u32 s21, s11, 0
	v_mul_u32_u24_e32 v130, 0x556, v1
	v_mov_b32_e32 v3, 0
	s_add_u32 s22, s20, 0x1000
	v_or_b32_sdwa v82, s28, v120 dst_sel:DWORD dst_unused:UNUSED_PAD src0_sel:DWORD src1_sel:WORD_1
	s_movk_i32 s3, 0x300
	v_mov_b64_e32 v[92:93], s[4:5]
	v_mul_lo_u16_sdwa v84, v130, v94 dst_sel:DWORD dst_unused:UNUSED_PAD src0_sel:WORD_1 src1_sel:DWORD
	v_or_b32_e32 v134, 0x400, v0
	s_addc_u32 s23, s21, 0
	v_mad_i64_i32 v[76:77], s[4:5], v82, s3, v[92:93]
	v_lshlrev_b32_e32 v80, 1, v124
	v_mov_b32_e32 v81, v3
	v_mov_b64_e32 v[96:97], s[6:7]
	v_sub_u16_e32 v86, v1, v84
	v_mul_u32_u24_e32 v132, 0x556, v134
	v_add_u32_e32 v100, 0x3000, v2
	v_add_u32_e32 v118, 0x6000, v2
	global_load_dwordx4 v[64:67], v2, s[20:21]
	global_load_dwordx4 v[52:55], v2, s[20:21] offset:1024
	global_load_dwordx4 v[68:71], v100, s[20:21]
	global_load_dwordx4 v[56:59], v100, s[20:21] offset:1024
	global_load_dwordx4 v[72:75], v118, s[20:21]
	global_load_dwordx4 v[60:63], v118, s[20:21] offset:1024
	global_load_dwordx4 v[40:43], v2, s[20:21] offset:2048
	global_load_dwordx4 v[16:19], v2, s[20:21] offset:3072
	global_load_dwordx4 v[44:47], v100, s[20:21] offset:2048
	global_load_dwordx4 v[20:23], v100, s[20:21] offset:3072
	global_load_dwordx4 v[48:51], v118, s[20:21] offset:2048
	global_load_dwordx4 v[24:27], v118, s[20:21] offset:3072
	s_add_u32 s20, s20, 0x1400
	v_lshl_add_u64 v[76:77], v[76:77], 0, v[80:81]
	v_mad_i64_i32 v[82:83], s[4:5], v82, s3, v[96:97]
	v_or_b32_sdwa v90, s28, v130 dst_sel:DWORD dst_unused:UNUSED_PAD src0_sel:DWORD src1_sel:WORD_1
	v_lshlrev_b16_e32 v131, 3, v86
	v_mul_lo_u16_sdwa v94, v132, v94 dst_sel:DWORD dst_unused:UNUSED_PAD src0_sel:WORD_1 src1_sel:DWORD
	s_addc_u32 s21, s21, 0
	global_load_dwordx4 v[28:31], v2, s[22:23]
	global_load_dwordx4 v[4:7], v2, s[20:21]
	global_load_dwordx4 v[32:35], v100, s[22:23]
	global_load_dwordx4 v[8:11], v100, s[20:21]
	global_load_dwordx4 v[36:39], v118, s[22:23]
	global_load_dwordx4 v[12:15], v118, s[20:21]
	v_lshl_add_u64 v[80:81], v[82:83], 0, v[80:81]
	global_load_dwordx4 v[76:79], v[76:77], off nt
	v_mad_i64_i32 v[84:85], s[4:5], v90, s3, v[92:93]
	v_lshlrev_b32_e32 v88, 1, v131
	v_mov_b32_e32 v89, v3
	v_sub_u16_e32 v94, v134, v94
	global_load_dwordx4 v[80:83], v[80:81], off nt
	v_lshl_add_u64 v[84:85], v[84:85], 0, v[88:89]
	v_mad_i64_i32 v[90:91], s[4:5], v90, s3, v[96:97]
	v_or_b32_sdwa v101, s28, v132 dst_sel:DWORD dst_unused:UNUSED_PAD src0_sel:DWORD src1_sel:WORD_1
	v_lshlrev_b16_e32 v133, 3, v94
	global_load_dwordx4 v[84:87], v[84:85], off nt
	v_lshl_add_u64 v[88:89], v[90:91], 0, v[88:89]
	v_mad_i64_i32 v[92:93], s[4:5], v101, s3, v[92:93]
	v_lshlrev_b32_e32 v98, 1, v133
	v_mov_b32_e32 v99, v3
	global_load_dwordx4 v[88:91], v[88:89], off nt
	v_lshl_add_u64 v[92:93], v[92:93], 0, v[98:99]
	v_mad_i64_i32 v[96:97], s[4:5], v101, s3, v[96:97]
	global_load_dwordx4 v[92:95], v[92:93], off nt
	v_lshl_add_u64 v[96:97], v[96:97], 0, v[98:99]
	v_and_b32_e32 v136, 15, v0
	global_load_dwordx4 v[96:99], v[96:97], off nt
	v_lshrrev_b32_e32 v101, 2, v0
	v_and_b32_e32 v135, 12, v101
	v_lshlrev_b32_e32 v102, 2, v136
	v_mov_b32_e32 v103, v3
	v_mad_u32_u24 v125, v121, 3, 2
	v_mul_u32_u24_e32 v144, 48, v121
	v_mad_u32_u24 v139, v121, 3, 1
	v_or_b32_e32 v137, s28, v135
	v_lshl_add_u64 v[102:103], s[8:9], 0, v[102:103]
	v_lshlrev_b32_e32 v104, 6, v125
	v_mov_b32_e32 v105, v3
	v_lshlrev_b32_e32 v106, 2, v144
	v_mov_b32_e32 v107, v3
	v_lshlrev_b32_e32 v116, 6, v139
	v_mov_b32_e32 v117, v3
	v_lshl_add_u64 v[104:105], v[102:103], 0, v[104:105]
	s_movk_i32 s3, 0x600
	v_lshl_add_u64 v[106:107], v[102:103], 0, v[106:107]
	v_or_b32_e32 v141, 3, v137
	v_lshl_add_u64 v[102:103], v[102:103], 0, v[116:117]
	v_mad_i64_i32 v[108:109], s[4:5], v137, s3, v[106:107]
	v_or_b32_e32 v138, 1, v137
	v_or_b32_e32 v140, 2, v137
	v_mad_i64_i32 v[128:129], s[4:5], v141, s3, v[102:103]
	v_mad_i64_i32 v[110:111], s[4:5], v138, s3, v[106:107]
	v_mad_i64_i32 v[112:113], s[4:5], v140, s3, v[106:107]
	v_mad_i64_i32 v[114:115], s[4:5], v141, s3, v[106:107]
	v_mad_i64_i32 v[116:117], s[4:5], v137, s3, v[102:103]
	v_mad_i64_i32 v[122:123], s[4:5], v138, s3, v[102:103]
	v_mad_i64_i32 v[126:127], s[4:5], v140, s3, v[102:103]
	global_load_dword v165, v[108:109], off nt
	global_load_dword v164, v[110:111], off nt
	global_load_dword v163, v[112:113], off nt
	global_load_dword v162, v[114:115], off nt
	global_load_dword v157, v[116:117], off nt
	global_load_dword v156, v[122:123], off nt
	global_load_dword v155, v[126:127], off nt
	global_load_dword v154, v[128:129], off nt
	v_or_b32_e32 v128, 16, v137
	v_or_b32_e32 v129, 17, v137
	v_or_b32_e32 v142, 18, v137
	v_or_b32_e32 v143, 19, v137
	v_mad_i64_i32 v[108:109], s[4:5], v137, s3, v[104:105]
	v_mad_i64_i32 v[116:117], s[4:5], v128, s3, v[106:107]
	v_mad_i64_i32 v[122:123], s[4:5], v129, s3, v[106:107]
	v_mad_i64_i32 v[126:127], s[4:5], v142, s3, v[106:107]
	v_mad_i64_i32 v[106:107], s[4:5], v143, s3, v[106:107]
	v_mad_i64_i32 v[110:111], s[4:5], v138, s3, v[104:105]
	v_mad_i64_i32 v[112:113], s[4:5], v140, s3, v[104:105]
	v_mad_i64_i32 v[114:115], s[4:5], v141, s3, v[104:105]
	global_load_dword v150, v[108:109], off nt
	global_load_dword v148, v[110:111], off nt
	global_load_dword v147, v[112:113], off nt
	global_load_dword v146, v[114:115], off nt
	global_load_dword v170, v[116:117], off nt
	global_load_dword v169, v[122:123], off nt
	global_load_dword v168, v[126:127], off nt
	global_load_dword v167, v[106:107], off nt
	v_mad_i64_i32 v[106:107], s[4:5], v128, s3, v[102:103]
	v_mad_i64_i32 v[108:109], s[4:5], v129, s3, v[102:103]
	v_mad_i64_i32 v[110:111], s[4:5], v142, s3, v[102:103]
	v_mad_i64_i32 v[102:103], s[4:5], v143, s3, v[102:103]
	v_mad_i64_i32 v[112:113], s[4:5], v128, s3, v[104:105]
	v_mad_i64_i32 v[114:115], s[4:5], v129, s3, v[104:105]
	v_mad_i64_i32 v[116:117], s[4:5], v142, s3, v[104:105]
	v_mad_i64_i32 v[104:105], s[4:5], v143, s3, v[104:105]
	global_load_dword v161, v[106:107], off nt
	global_load_dword v160, v[108:109], off nt
	global_load_dword v159, v[110:111], off nt
	global_load_dword v158, v[102:103], off nt
	global_load_dword v153, v[112:113], off nt
	global_load_dword v152, v[114:115], off nt
	global_load_dword v151, v[116:117], off nt
	global_load_dword v149, v[104:105], off nt
	s_load_dwordx2 s[4:5], s[0:1], 0x60
	s_load_dwordx8 s[20:27], s[0:1], 0x40
	s_movk_i32 s0, 0x188
	v_mul_u32_u24_sdwa v102, v120, s0 dst_sel:DWORD dst_unused:UNUSED_PAD src0_sel:WORD_1 src1_sel:DWORD
	v_add_lshl_u32 v102, v102, v124, 1
	v_lshl_add_u64 v[122:123], s[10:11], 0, v[2:3]
	v_lshrrev_b32_e32 v2, 1, v0
	s_waitcnt vmcnt(29)
	ds_write_b128 v102, v[76:79]
	s_waitcnt vmcnt(28)
	ds_write_b128 v102, v[80:83] offset:25088
	v_mul_u32_u24_sdwa v76, v130, s0 dst_sel:DWORD dst_unused:UNUSED_PAD src0_sel:WORD_1 src1_sel:DWORD
	v_and_b32_e32 v2, 24, v2
	v_add_lshl_u32 v76, v76, v131, 1
	v_mad_i64_i32 v[116:117], s[6:7], v137, s3, 0
	v_mad_i64_i32 v[114:115], s[6:7], v138, s3, 0
	v_mad_i64_i32 v[112:113], s[6:7], v140, s3, 0
	v_mad_i64_i32 v[110:111], s[6:7], v141, s3, 0
	v_mad_i64_i32 v[108:109], s[6:7], v128, s3, 0
	v_mad_i64_i32 v[106:107], s[6:7], v129, s3, 0
	v_mad_i64_i32 v[104:105], s[6:7], v142, s3, 0
	v_mad_i64_i32 v[102:103], s[6:7], v143, s3, 0
	s_bfe_u32 s3, s2, 0x10003
	v_mad_u32_u24 v138, v136, s0, v2
	s_waitcnt vmcnt(27)
	ds_write_b128 v76, v[84:87]
	s_waitcnt vmcnt(26)
	ds_write_b128 v76, v[88:91] offset:25088
	v_mul_u32_u24_sdwa v76, v132, s0 dst_sel:DWORD dst_unused:UNUSED_PAD src0_sel:WORD_1 src1_sel:DWORD
	s_cmp_eq_u32 s3, 0
	s_mulk_i32 s3, 0x180
	v_lshlrev_b32_e32 v137, 1, v138
	v_add_lshl_u32 v76, v76, v133, 1
	v_add_u32_e32 v2, s3, v137
	s_waitcnt vmcnt(25)
	ds_write_b128 v76, v[92:95]
	s_waitcnt vmcnt(24)
	ds_write_b128 v76, v[96:99] offset:25088
	s_waitcnt lgkmcnt(0)
	s_barrier
	ds_read_b128 v[76:79], v2
	ds_read_b128 v[80:83], v2 offset:64
	ds_read_b128 v[84:87], v2 offset:12544
	ds_read_b128 v[88:91], v2 offset:12608
	ds_read_b128 v[92:95], v2 offset:128
	ds_read_b128 v[96:99], v2 offset:192
	ds_read_b128 v[126:129], v2 offset:12672
	ds_read_b128 v[130:133], v2 offset:12736
	ds_read_b128 v[140:143], v2 offset:256
	ds_read_b128 v[172:175], v2 offset:320
	ds_read_b128 v[176:179], v2 offset:12800
	ds_read_b128 v[180:183], v2 offset:12864
	v_mov_b32_e32 v101, v3
	v_mov_b32_e32 v119, v3
	s_mov_b32 s1, 0
	v_lshl_add_u64 v[100:101], s[10:11], 0, v[100:101]
	v_lshl_add_u64 v[118:119], s[10:11], 0, v[118:119]
	s_cselect_b32 s0, 0x1800, 0
	v_lshl_add_u64 v[122:123], v[122:123], 0, s[0:1]
	v_lshl_add_u64 v[100:101], v[100:101], 0, s[0:1]
	v_lshl_add_u64 v[118:119], v[118:119], 0, s[0:1]
	s_setprio 1
	s_waitcnt lgkmcnt(11)
	v_mfma_f32_16x16x32_bf16 v[184:187], v[76:79], v[64:67], 0
	s_waitcnt lgkmcnt(9)
	v_mfma_f32_16x16x32_bf16 v[64:67], v[84:87], v[64:67], 0
	v_mfma_f32_16x16x32_bf16 v[188:191], v[76:79], v[68:71], 0
	v_mfma_f32_16x16x32_bf16 v[68:71], v[84:87], v[68:71], 0
	v_mfma_f32_16x16x32_bf16 v[76:79], v[76:79], v[72:75], 0
	v_mfma_f32_16x16x32_bf16 v[72:75], v[84:87], v[72:75], 0
	s_setprio 0
	global_load_dwordx4 v[84:87], v[122:123], off
	global_load_dwordx4 v[192:195], v[100:101], off
	global_load_dwordx4 v[196:199], v[118:119], off
	s_setprio 1
	v_mfma_f32_16x16x32_bf16 v[184:187], v[80:83], v[52:55], v[184:187]
	s_waitcnt lgkmcnt(8)
	v_mfma_f32_16x16x32_bf16 v[52:55], v[88:91], v[52:55], v[64:67]
	v_mfma_f32_16x16x32_bf16 v[64:67], v[80:83], v[56:59], v[188:191]
	v_mfma_f32_16x16x32_bf16 v[56:59], v[88:91], v[56:59], v[68:71]
	v_mfma_f32_16x16x32_bf16 v[68:71], v[80:83], v[60:63], v[76:79]
	v_mfma_f32_16x16x32_bf16 v[60:63], v[88:91], v[60:63], v[72:75]
	s_setprio 0
	s_nop 1
	global_load_dwordx4 v[72:75], v[122:123], off offset:1024
	global_load_dwordx4 v[76:79], v[100:101], off offset:1024
	global_load_dwordx4 v[80:83], v[118:119], off offset:1024
	s_setprio 1
	s_waitcnt lgkmcnt(7)
	v_mfma_f32_16x16x32_bf16 v[88:91], v[92:95], v[40:43], v[184:187]
	s_waitcnt lgkmcnt(5)
	v_mfma_f32_16x16x32_bf16 v[40:43], v[126:129], v[40:43], v[52:55]
	v_mfma_f32_16x16x32_bf16 v[52:55], v[92:95], v[44:47], v[64:67]
	v_mfma_f32_16x16x32_bf16 v[44:47], v[126:129], v[44:47], v[56:59]
	v_mfma_f32_16x16x32_bf16 v[56:59], v[92:95], v[48:51], v[68:71]
	v_mfma_f32_16x16x32_bf16 v[48:51], v[126:129], v[48:51], v[60:63]
	s_setprio 0
	s_nop 1
	global_load_dwordx4 v[60:63], v[122:123], off offset:2048
	global_load_dwordx4 v[64:67], v[100:101], off offset:2048
	global_load_dwordx4 v[68:71], v[118:119], off offset:2048
	s_setprio 1
	v_mfma_f32_16x16x32_bf16 v[88:91], v[96:99], v[16:19], v[88:91]
	s_waitcnt lgkmcnt(4)
	v_mfma_f32_16x16x32_bf16 v[16:19], v[130:133], v[16:19], v[40:43]
	v_mfma_f32_16x16x32_bf16 v[40:43], v[96:99], v[20:23], v[52:55]
	v_mfma_f32_16x16x32_bf16 v[20:23], v[130:133], v[20:23], v[44:47]
	v_mfma_f32_16x16x32_bf16 v[44:47], v[96:99], v[24:27], v[56:59]
	v_mfma_f32_16x16x32_bf16 v[24:27], v[130:133], v[24:27], v[48:51]
	s_setprio 0
	s_nop 1
	global_load_dwordx4 v[48:51], v[122:123], off offset:3072
	global_load_dwordx4 v[52:55], v[100:101], off offset:3072
	global_load_dwordx4 v[56:59], v[118:119], off offset:3072
	s_setprio 1
	s_waitcnt lgkmcnt(3)
	v_mfma_f32_16x16x32_bf16 v[88:91], v[140:143], v[28:31], v[88:91]
	s_waitcnt lgkmcnt(1)
	v_mfma_f32_16x16x32_bf16 v[16:19], v[176:179], v[28:31], v[16:19]
	v_mfma_f32_16x16x32_bf16 v[28:31], v[140:143], v[32:35], v[40:43]
	v_mfma_f32_16x16x32_bf16 v[20:23], v[176:179], v[32:35], v[20:23]
	v_mfma_f32_16x16x32_bf16 v[32:35], v[140:143], v[36:39], v[44:47]
	v_mfma_f32_16x16x32_bf16 v[24:27], v[176:179], v[36:39], v[24:27]
	s_setprio 0
	s_movk_i32 s0, 0x1000
	v_add_co_u32_e32 v92, vcc, s0, v122
	s_nop 1
	v_addc_co_u32_e32 v93, vcc, 0, v123, vcc
	v_add_co_u32_e32 v94, vcc, s0, v100
	s_nop 1
	v_addc_co_u32_e32 v95, vcc, 0, v101, vcc
	v_add_co_u32_e32 v96, vcc, s0, v118
	global_load_dwordx4 v[36:39], v[92:93], off
	global_load_dwordx4 v[40:43], v[94:95], off
	v_addc_co_u32_e32 v97, vcc, 0, v119, vcc
	global_load_dwordx4 v[44:47], v[96:97], off
	s_setprio 1
	v_mfma_f32_16x16x32_bf16 v[88:91], v[172:175], v[4:7], v[88:91]
	s_waitcnt lgkmcnt(0)
	v_mfma_f32_16x16x32_bf16 v[4:7], v[180:183], v[4:7], v[16:19]
	v_mfma_f32_16x16x32_bf16 v[16:19], v[172:175], v[8:11], v[28:31]
	v_mfma_f32_16x16x32_bf16 v[8:11], v[180:183], v[8:11], v[20:23]
	v_mfma_f32_16x16x32_bf16 v[20:23], v[172:175], v[12:15], v[32:35]
	v_mfma_f32_16x16x32_bf16 v[12:15], v[180:183], v[12:15], v[24:27]
	s_setprio 0
	s_nop 1
	global_load_dwordx4 v[24:27], v[92:93], off offset:1024
	global_load_dwordx4 v[28:31], v[94:95], off offset:1024
	global_load_dwordx4 v[32:35], v[96:97], off offset:1024
	s_cselect_b32 s3, 0x180, 0
	v_add_u32_e32 v2, s3, v137
	ds_read_b128 v[92:95], v2
	ds_read_b128 v[96:99], v2 offset:64
	ds_read_b128 v[126:129], v2 offset:12544
	ds_read_b128 v[130:133], v2 offset:12608
	ds_read_b128 v[140:143], v2 offset:128
	ds_read_b128 v[172:175], v2 offset:192
	ds_read_b128 v[176:179], v2 offset:12672
	ds_read_b128 v[180:183], v2 offset:12736
	ds_read_b128 v[184:187], v2 offset:256
	ds_read_b128 v[188:191], v2 offset:320
	ds_read_b128 v[200:203], v2 offset:12800
	ds_read_b128 v[204:207], v2 offset:12864
	s_setprio 1
	s_waitcnt vmcnt(17) lgkmcnt(11)
	v_mfma_f32_16x16x32_bf16 v[88:91], v[92:95], v[84:87], v[88:91]
	s_waitcnt lgkmcnt(9)
	v_mfma_f32_16x16x32_bf16 v[4:7], v[126:129], v[84:87], v[4:7]
	s_waitcnt vmcnt(16)
	v_mfma_f32_16x16x32_bf16 v[16:19], v[92:95], v[192:195], v[16:19]
	v_mfma_f32_16x16x32_bf16 v[8:11], v[126:129], v[192:195], v[8:11]
	s_waitcnt vmcnt(15)
	v_mfma_f32_16x16x32_bf16 v[20:23], v[92:95], v[196:199], v[20:23]
	v_mfma_f32_16x16x32_bf16 v[12:15], v[126:129], v[196:199], v[12:15]
	s_setprio 0
	s_setprio 1
	s_waitcnt vmcnt(14)
	v_mfma_f32_16x16x32_bf16 v[84:87], v[96:99], v[72:75], v[88:91]
	s_waitcnt lgkmcnt(8)
	v_mfma_f32_16x16x32_bf16 v[4:7], v[130:133], v[72:75], v[4:7]
	s_waitcnt vmcnt(13)
	v_mfma_f32_16x16x32_bf16 v[16:19], v[96:99], v[76:79], v[16:19]
	v_mfma_f32_16x16x32_bf16 v[8:11], v[130:133], v[76:79], v[8:11]
	s_waitcnt vmcnt(12)
	v_mfma_f32_16x16x32_bf16 v[20:23], v[96:99], v[80:83], v[20:23]
	v_mfma_f32_16x16x32_bf16 v[12:15], v[130:133], v[80:83], v[12:15]
	s_setprio 0
	s_setprio 1
	s_waitcnt vmcnt(11) lgkmcnt(7)
	v_mfma_f32_16x16x32_bf16 v[72:75], v[140:143], v[60:63], v[84:87]
	s_waitcnt lgkmcnt(5)
	v_mfma_f32_16x16x32_bf16 v[4:7], v[176:179], v[60:63], v[4:7]
	s_waitcnt vmcnt(10)
	v_mfma_f32_16x16x32_bf16 v[16:19], v[140:143], v[64:67], v[16:19]
	v_mfma_f32_16x16x32_bf16 v[8:11], v[176:179], v[64:67], v[8:11]
	s_waitcnt vmcnt(9)
	v_mfma_f32_16x16x32_bf16 v[20:23], v[140:143], v[68:71], v[20:23]
	v_mfma_f32_16x16x32_bf16 v[12:15], v[176:179], v[68:71], v[12:15]
	s_setprio 0
	s_setprio 1
	s_waitcnt vmcnt(8)
	v_mfma_f32_16x16x32_bf16 v[60:63], v[172:175], v[48:51], v[72:75]
	s_waitcnt lgkmcnt(4)
	v_mfma_f32_16x16x32_bf16 v[4:7], v[180:183], v[48:51], v[4:7]
	s_waitcnt vmcnt(7)
	v_mfma_f32_16x16x32_bf16 v[16:19], v[172:175], v[52:55], v[16:19]
	v_mfma_f32_16x16x32_bf16 v[8:11], v[180:183], v[52:55], v[8:11]
	s_waitcnt vmcnt(6)
	v_mfma_f32_16x16x32_bf16 v[20:23], v[172:175], v[56:59], v[20:23]
	v_mfma_f32_16x16x32_bf16 v[12:15], v[180:183], v[56:59], v[12:15]
	s_setprio 0
	s_setprio 1
	s_waitcnt vmcnt(5) lgkmcnt(3)
	v_mfma_f32_16x16x32_bf16 v[48:51], v[184:187], v[36:39], v[60:63]
	s_waitcnt lgkmcnt(1)
	v_mfma_f32_16x16x32_bf16 v[4:7], v[200:203], v[36:39], v[4:7]
	s_waitcnt vmcnt(4)
	v_mfma_f32_16x16x32_bf16 v[16:19], v[184:187], v[40:43], v[16:19]
	v_mfma_f32_16x16x32_bf16 v[8:11], v[200:203], v[40:43], v[8:11]
	s_waitcnt vmcnt(3)
	v_mfma_f32_16x16x32_bf16 v[20:23], v[184:187], v[44:47], v[20:23]
	v_mfma_f32_16x16x32_bf16 v[12:15], v[200:203], v[44:47], v[12:15]
	s_setprio 0
	s_setprio 1
	s_waitcnt vmcnt(2)
	v_mfma_f32_16x16x32_bf16 v[74:77], v[188:191], v[24:27], v[48:51]
	s_waitcnt lgkmcnt(0)
	v_mfma_f32_16x16x32_bf16 v[92:95], v[204:207], v[24:27], v[4:7]
	s_waitcnt vmcnt(1)
	v_mfma_f32_16x16x32_bf16 v[70:73], v[188:191], v[28:31], v[16:19]
	v_mfma_f32_16x16x32_bf16 v[86:89], v[204:207], v[28:31], v[8:11]
	s_waitcnt vmcnt(0)
	v_mfma_f32_16x16x32_bf16 v[82:85], v[188:191], v[32:35], v[20:23]
	v_mfma_f32_16x16x32_bf16 v[78:81], v[204:207], v[32:35], v[12:15]
	s_setprio 0
	v_or_b32_e32 v120, v144, v136
	v_lshlrev_b32_e32 v2, 2, v120
	global_load_dword v96, v2, s[14:15]
	v_lshl_or_b32 v122, v139, 4, v136
	v_lshlrev_b32_e32 v4, 2, v122
	global_load_dword v119, v4, s[14:15]
	s_bfe_u32 s8, s2, 0x20003
	s_movk_i32 s2, 0x310
	v_mov_b32_e32 v4, 0x930
	v_lshl_or_b32 v118, v125, 4, v136
	v_mad_u32_u24 v142, v135, s2, v4
	v_lshlrev_b32_e32 v4, 2, v118
	global_load_dword v166, v4, s[14:15]
	v_mul_u32_u24_e32 v171, 0x1200, v121
	s_mul_i32 s3, s8, 0x1800
	v_or_b32_e32 v9, v171, v145
	s_add_u32 s6, s12, s3
	v_lshlrev_b32_e32 v124, 3, v9
	s_addc_u32 s7, s13, 0
	v_mov_b32_e32 v97, 0xc400
	v_mov_b32_e32 v2, 0x620
	v_add_u32_e32 v100, 0x3000, v124
	s_add_u32 s10, s6, 0x1000
	v_mov_b32_e32 v6, 0x3100
	v_mov_b32_e32 v7, 0x3410
	v_mov_b32_e32 v8, 0x3720
	v_lshl_or_b32 v123, v120, 1, v97
	v_mad_u32_u24 v143, v135, s2, v2
	v_lshlrev_b32_e32 v2, 4, v9
	v_add_u32_e32 v98, 0x6000, v124
	v_lshlrev_b32_e32 v4, 1, v100
	s_addc_u32 s11, s7, 0
	v_mad_u32_u24 v144, v135, s2, s2
	v_mad_u32_u24 v141, v135, s2, v6
	v_mad_u32_u24 v140, v135, s2, v7
	v_mad_u32_u24 v132, v135, s2, v8
	v_mad_u32_u24 v126, v135, s2, v123
	v_lshlrev_b32_e32 v90, 1, v98
	global_load_dwordx4 v[50:53], v2, s[6:7]
	global_load_dwordx4 v[30:33], v2, s[6:7] offset:1024
	global_load_dwordx4 v[18:21], v2, s[6:7] offset:2048
	global_load_dwordx4 v[6:9], v2, s[6:7] offset:3072
	global_load_dwordx4 v[58:61], v4, s[6:7]
	global_load_dwordx4 v[42:45], v4, s[6:7] offset:1024
	global_load_dwordx4 v[54:57], v90, s[6:7]
	global_load_dwordx4 v[34:37], v90, s[6:7] offset:1024
	global_load_dwordx4 v[26:29], v4, s[6:7] offset:2048
	global_load_dwordx4 v[14:17], v4, s[6:7] offset:3072
	global_load_dwordx4 v[22:25], v90, s[6:7] offset:2048
	global_load_dwordx4 v[10:13], v90, s[6:7] offset:3072
	s_add_u32 s6, s6, 0x1400
	v_add_u32_e32 v127, v123, v144
	v_add_u32_e32 v128, v123, v143
	v_add_u32_e32 v129, v123, v142
	v_add_u32_e32 v130, v123, v141
	v_add_u32_e32 v131, v123, v140
	s_addc_u32 s7, s7, 0
	global_load_dwordx4 v[62:65], v2, s[10:11]
	global_load_dwordx4 v[46:49], v2, s[6:7]
	global_load_dwordx4 v[66:69], v4, s[10:11]
	global_load_dwordx4 v[38:41], v4, s[6:7]
	v_mov_b32_e32 v5, v3
	v_mov_b32_e32 v91, v3
	v_mov_b32_e32 v101, v3
	v_mov_b32_e32 v99, v3
	s_waitcnt vmcnt(18)
	v_add_f32_e32 v74, v96, v74
	v_add_f32_e32 v75, v96, v75
	v_add_f32_e32 v76, v96, v76
	v_add_f32_e32 v77, v96, v77
	v_add_f32_e32 v92, v96, v92
	v_add_f32_e32 v93, v96, v93
	v_add_f32_e32 v94, v96, v94
	v_cvt_pk_bf16_f32 v74, v74, s0
	v_cvt_pk_bf16_f32 v75, v75, s0
	v_cvt_pk_bf16_f32 v76, v76, s0
	v_cvt_pk_bf16_f32 v77, v77, s0
	v_cvt_pk_bf16_f32 v92, v92, s0
	v_cvt_pk_bf16_f32 v93, v93, s0
	v_cvt_pk_bf16_f32 v94, v94, s0
	ds_write_b16 v126, v74
	ds_write_b16 v127, v75
	ds_write_b16 v128, v76
	ds_write_b16 v129, v77
	ds_write_b16 v130, v92
	ds_write_b16 v131, v93
	v_add_u32_e32 v74, v123, v132
	v_mov_b32_e32 v75, 0x3a30
	ds_write_b16 v74, v94
	v_add_f32_e32 v74, v96, v95
	v_mad_u32_u24 v133, v135, s2, v75
	v_cvt_pk_bf16_f32 v74, v74, s0
	v_add_u32_e32 v75, v123, v133
	v_lshl_add_u32 v92, v122, 1, v97
	s_waitcnt vmcnt(17)
	v_add_f32_e32 v70, v119, v70
	ds_write_b16 v75, v74
	v_cvt_pk_bf16_f32 v70, v70, s0
	v_mad_u32_u24 v74, v135, s2, v92
	ds_write_b16 v74, v70
	v_add_f32_e32 v70, v119, v71
	v_cvt_pk_bf16_f32 v70, v70, s0
	v_add_u32_e32 v71, v92, v144
	ds_write_b16 v71, v70
	v_add_f32_e32 v70, v119, v72
	v_cvt_pk_bf16_f32 v70, v70, s0
	v_add_u32_e32 v71, v92, v143
	ds_write_b16 v71, v70
	v_add_f32_e32 v93, v119, v73
	global_load_dwordx4 v[74:77], v90, s[10:11]
	global_load_dwordx4 v[70:73], v90, s[6:7]
	v_cvt_pk_bf16_f32 v93, v93, s0
	v_add_u32_e32 v94, v92, v142
	v_add_f32_e32 v86, v119, v86
	ds_write_b16 v94, v93
	v_cvt_pk_bf16_f32 v86, v86, s0
	v_add_u32_e32 v93, v92, v141
	ds_write_b16 v93, v86
	v_add_f32_e32 v86, v119, v87
	v_cvt_pk_bf16_f32 v86, v86, s0
	v_add_u32_e32 v87, v92, v140
	ds_write_b16 v87, v86
	v_add_f32_e32 v86, v119, v88
	v_cvt_pk_bf16_f32 v86, v86, s0
	v_add_u32_e32 v87, v92, v132
	ds_write_b16 v87, v86
	v_add_f32_e32 v86, v119, v89
	v_cvt_pk_bf16_f32 v86, v86, s0
	v_add_u32_e32 v87, v92, v133
	ds_write_b16 v87, v86
	v_lshl_add_u32 v86, v118, 1, v97
	s_waitcnt vmcnt(18)
	v_add_f32_e32 v82, v166, v82
	v_cvt_pk_bf16_f32 v82, v82, s0
	v_mad_u32_u24 v87, v135, s2, v86
	ds_write_b16 v87, v82
	v_add_f32_e32 v82, v166, v83
	v_cvt_pk_bf16_f32 v82, v82, s0
	v_add_u32_e32 v83, v86, v144
	ds_write_b16 v83, v82
	v_add_f32_e32 v82, v166, v84
	v_cvt_pk_bf16_f32 v82, v82, s0
	v_add_u32_e32 v83, v86, v143
	ds_write_b16 v83, v82
	v_add_f32_e32 v82, v166, v85
	v_cvt_pk_bf16_f32 v82, v82, s0
	v_add_u32_e32 v83, v86, v142
	v_add_f32_e32 v78, v166, v78
	ds_write_b16 v83, v82
	v_cvt_pk_bf16_f32 v78, v78, s0
	v_add_u32_e32 v82, v86, v141
	ds_write_b16 v82, v78
	v_add_f32_e32 v78, v166, v79
	v_cvt_pk_bf16_f32 v78, v78, s0
	v_add_u32_e32 v79, v86, v140
	ds_write_b16 v79, v78
	v_add_f32_e32 v78, v166, v80
	v_cvt_pk_bf16_f32 v78, v78, s0
	v_add_u32_e32 v79, v86, v132
	ds_write_b16 v79, v78
	v_add_f32_e32 v78, v166, v81
	v_cvt_pk_bf16_f32 v78, v78, s0
	v_add_u32_e32 v79, v86, v133
	v_mov_b32_e32 v123, v3
	v_mov_b32_e32 v119, v3
	ds_write_b16 v79, v78
	v_lshl_add_u64 v[126:127], s[12:13], 0, v[2:3]
	v_lshl_add_u64 v[128:129], s[12:13], 0, v[4:5]
	v_lshl_add_u64 v[130:131], s[12:13], 0, v[90:91]
	s_movk_i32 s2, 0x5f00
	v_mov_b32_e32 v2, v3
	v_mov_b32_e32 v4, v3
	v_mov_b32_e32 v78, v3
	v_mov_b32_e32 v79, v3
	v_mov_b32_e32 v80, v3
	v_mov_b32_e32 v81, v3
	v_mov_b32_e32 v82, v3
	v_mov_b32_e32 v83, v3
	v_mov_b32_e32 v84, v3
	v_mov_b32_e32 v85, v3
	v_mov_b32_e32 v86, v3
	v_mov_b32_e32 v87, v3
	v_mov_b32_e32 v88, v3
	v_mov_b32_e32 v89, v3
	v_mov_b32_e32 v90, v3
	v_mov_b32_e32 v92, v3
	v_mov_b32_e32 v93, v3
	v_mov_b32_e32 v94, v3
	v_mov_b32_e32 v95, v3
	v_mov_b32_e32 v96, v3
	v_mov_b32_e32 v97, v3
	v_mul_u32_u24_e32 v166, 0x310, v135
	s_waitcnt lgkmcnt(0)
	s_barrier

_Z12chain_kernelILi1EEv9ChainArgs:
	s_load_dwordx16 s[4:19], s[0:1], 0x0
	v_lshrrev_b32_e32 v158, 6, v0
	v_and_b32_e32 v131, 63, v0
	v_mul_u32_u24_e32 v1, 0x900, v158
	v_or_b32_e32 v1, v1, v131
	v_mul_u32_u24_e32 v124, 0x556, v0
	v_mov_b32_e32 v94, 48
	s_bfe_i32 s3, s2, 0x10003
	v_lshlrev_b32_e32 v2, 4, v1
	v_mul_lo_u16_sdwa v1, v124, v94 dst_sel:DWORD dst_unused:UNUSED_PAD src0_sel:WORD_1 src1_sel:DWORD
	v_or_b32_e32 v125, 0x200, v0
	s_lshl_b32 s28, s2, 5
	s_and_b32 s3, s3, 0x1800
	v_sub_u16_e32 v1, v0, v1
	v_mul_u32_u24_e32 v144, 0x556, v125
	s_waitcnt lgkmcnt(0)
	s_add_u32 s20, s10, s3
	v_lshlrev_b16_e32 v130, 3, v1
	v_mul_lo_u16_sdwa v1, v144, v94 dst_sel:DWORD dst_unused:UNUSED_PAD src0_sel:WORD_1 src1_sel:DWORD
	s_addc_u32 s21, s11, 0
	v_sub_u16_e32 v1, v125, v1
	v_mov_b32_e32 v3, 0
	s_add_u32 s22, s20, 0x1000
	v_or_b32_sdwa v82, s28, v124 dst_sel:DWORD dst_unused:UNUSED_PAD src0_sel:DWORD src1_sel:WORD_1
	s_movk_i32 s3, 0x300
	v_mov_b64_e32 v[92:93], s[4:5]
	v_lshlrev_b16_e32 v145, 3, v1
	v_or_b32_e32 v1, 0x400, v0
	s_addc_u32 s23, s21, 0
	v_mad_i64_i32 v[76:77], s[4:5], v82, s3, v[92:93]
	v_lshlrev_b32_e32 v80, 1, v130
	v_mov_b32_e32 v81, v3
	v_mov_b64_e32 v[96:97], s[6:7]
	v_mul_u32_u24_e32 v146, 0x556, v1
	v_add_u32_e32 v126, 0x3000, v2
	v_add_u32_e32 v128, 0x6000, v2
	global_load_dwordx4 v[64:67], v2, s[20:21]
	global_load_dwordx4 v[52:55], v2, s[20:21] offset:1024
	global_load_dwordx4 v[68:71], v126, s[20:21]
	global_load_dwordx4 v[56:59], v126, s[20:21] offset:1024
	global_load_dwordx4 v[72:75], v128, s[20:21]
	global_load_dwordx4 v[60:63], v128, s[20:21] offset:1024
	global_load_dwordx4 v[40:43], v2, s[20:21] offset:2048
	global_load_dwordx4 v[16:19], v2, s[20:21] offset:3072
	global_load_dwordx4 v[44:47], v126, s[20:21] offset:2048
	global_load_dwordx4 v[20:23], v126, s[20:21] offset:3072
	global_load_dwordx4 v[48:51], v128, s[20:21] offset:2048
	global_load_dwordx4 v[24:27], v128, s[20:21] offset:3072
	s_add_u32 s20, s20, 0x1400
	v_lshl_add_u64 v[76:77], v[76:77], 0, v[80:81]
	v_mad_i64_i32 v[82:83], s[4:5], v82, s3, v[96:97]
	v_or_b32_sdwa v90, s28, v144 dst_sel:DWORD dst_unused:UNUSED_PAD src0_sel:DWORD src1_sel:WORD_1
	v_mul_lo_u16_sdwa v94, v146, v94 dst_sel:DWORD dst_unused:UNUSED_PAD src0_sel:WORD_1 src1_sel:DWORD
	s_addc_u32 s21, s21, 0
	global_load_dwordx4 v[28:31], v2, s[22:23]
	global_load_dwordx4 v[4:7], v2, s[20:21]
	global_load_dwordx4 v[32:35], v126, s[22:23]
	global_load_dwordx4 v[8:11], v126, s[20:21]
	global_load_dwordx4 v[36:39], v128, s[22:23]
	global_load_dwordx4 v[12:15], v128, s[20:21]
	v_lshl_add_u64 v[80:81], v[82:83], 0, v[80:81]
	global_load_dwordx4 v[76:79], v[76:77], off nt
	v_mad_i64_i32 v[84:85], s[4:5], v90, s3, v[92:93]
	v_lshlrev_b32_e32 v88, 1, v145
	v_mov_b32_e32 v89, v3
	v_sub_u16_e32 v94, v1, v94
	global_load_dwordx4 v[80:83], v[80:81], off nt
	v_lshl_add_u64 v[84:85], v[84:85], 0, v[88:89]
	v_mad_i64_i32 v[90:91], s[4:5], v90, s3, v[96:97]
	v_or_b32_sdwa v100, s28, v146 dst_sel:DWORD dst_unused:UNUSED_PAD src0_sel:DWORD src1_sel:WORD_1
	v_lshlrev_b16_e32 v147, 3, v94
	global_load_dwordx4 v[84:87], v[84:85], off nt
	v_lshl_add_u64 v[88:89], v[90:91], 0, v[88:89]
	v_mad_i64_i32 v[92:93], s[4:5], v100, s3, v[92:93]
	v_lshlrev_b32_e32 v98, 1, v147
	v_mov_b32_e32 v99, v3
	global_load_dwordx4 v[88:91], v[88:89], off nt
	v_lshl_add_u64 v[92:93], v[92:93], 0, v[98:99]
	v_mad_i64_i32 v[96:97], s[4:5], v100, s3, v[96:97]
	global_load_dwordx4 v[92:95], v[92:93], off nt
	v_lshl_add_u64 v[96:97], v[96:97], 0, v[98:99]
	v_and_b32_e32 v171, 15, v0
	global_load_dwordx4 v[96:99], v[96:97], off nt
	v_bfe_u32 v170, v0, 4, 2
	v_lshlrev_b32_e32 v165, 2, v170
	v_lshlrev_b32_e32 v100, 2, v171
	v_mov_b32_e32 v101, v3
	v_mul_u32_u24_e32 v163, 48, v158
	v_mad_u32_u24 v162, v158, 3, 1
	v_or_b32_e32 v127, s28, v165
	v_lshl_add_u64 v[100:101], s[8:9], 0, v[100:101]
	v_mad_u32_u24 v159, v158, 3, 2
	v_lshlrev_b32_e32 v104, 2, v163
	v_mov_b32_e32 v105, v3
	v_lshlrev_b32_e32 v114, 6, v162
	v_mov_b32_e32 v115, v3
	v_lshlrev_b32_e32 v102, 6, v159
	v_mov_b32_e32 v103, v3
	v_lshl_add_u64 v[104:105], v[100:101], 0, v[104:105]
	s_movk_i32 s3, 0x600
	v_or_b32_e32 v137, 3, v127
	v_lshl_add_u64 v[132:133], v[100:101], 0, v[114:115]
	v_lshl_add_u64 v[102:103], v[100:101], 0, v[102:103]
	v_mad_i64_i32 v[106:107], s[4:5], v127, s3, v[104:105]
	v_or_b32_e32 v129, 1, v127
	v_or_b32_e32 v136, 2, v127
	v_mad_i64_i32 v[112:113], s[4:5], v137, s3, v[104:105]
	v_mad_i64_i32 v[100:101], s[4:5], v127, s3, v[132:133]
	v_mad_i64_i32 v[108:109], s[4:5], v129, s3, v[104:105]
	v_mad_i64_i32 v[110:111], s[4:5], v136, s3, v[104:105]
	v_mad_i64_i32 v[116:117], s[4:5], v129, s3, v[132:133]
	v_mad_i64_i32 v[122:123], s[4:5], v136, s3, v[132:133]
	v_mad_i64_i32 v[134:135], s[4:5], v137, s3, v[132:133]
	global_load_dword v118, v[106:107], off nt
	global_load_dword v119, v[108:109], off nt
	global_load_dword v114, v[110:111], off nt
	global_load_dword v115, v[112:113], off nt
	global_load_dword v120, v[100:101], off nt
	global_load_dword v121, v[116:117], off nt
	s_nop 0
	global_load_dword v112, v[122:123], off nt
	global_load_dword v113, v[134:135], off nt
	v_mad_i64_i32 v[100:101], s[4:5], v127, s3, v[102:103]
	v_mad_i64_i32 v[106:107], s[4:5], v129, s3, v[102:103]
	v_or_b32_e32 v129, 16, v127
	v_or_b32_e32 v140, 17, v127
	v_or_b32_e32 v141, 18, v127
	v_or_b32_e32 v127, 19, v127
	v_mad_i64_i32 v[108:109], s[4:5], v136, s3, v[102:103]
	v_mad_i64_i32 v[110:111], s[4:5], v137, s3, v[102:103]
	v_mad_i64_i32 v[134:135], s[4:5], v129, s3, v[104:105]
	v_mad_i64_i32 v[136:137], s[4:5], v140, s3, v[104:105]
	v_mad_i64_i32 v[138:139], s[4:5], v141, s3, v[104:105]
	v_mad_i64_i32 v[104:105], s[4:5], v127, s3, v[104:105]
	global_load_dword v122, v[100:101], off nt
	global_load_dword v123, v[106:107], off nt
	global_load_dword v116, v[108:109], off nt
	global_load_dword v117, v[110:111], off nt
	s_nop 0
	global_load_dword v106, v[134:135], off nt
	global_load_dword v107, v[136:137], off nt
	global_load_dword v100, v[138:139], off nt
	global_load_dword v101, v[104:105], off nt
	v_mad_i64_i32 v[104:105], s[4:5], v129, s3, v[132:133]
	v_mad_i64_i32 v[108:109], s[4:5], v140, s3, v[132:133]
	v_mad_i64_i32 v[134:135], s[4:5], v141, s3, v[132:133]
	v_mad_i64_i32 v[132:133], s[4:5], v127, s3, v[132:133]
	v_mad_i64_i32 v[136:137], s[4:5], v129, s3, v[102:103]
	v_mad_i64_i32 v[138:139], s[4:5], v140, s3, v[102:103]
	v_mad_i64_i32 v[140:141], s[4:5], v141, s3, v[102:103]
	v_mad_i64_i32 v[142:143], s[4:5], v127, s3, v[102:103]
	global_load_dword v110, v[104:105], off nt
	global_load_dword v111, v[108:109], off nt
	s_nop 0
	global_load_dword v104, v[134:135], off nt
	global_load_dword v105, v[132:133], off nt
	global_load_dword v108, v[136:137], off nt
	global_load_dword v109, v[138:139], off nt
	global_load_dword v102, v[140:141], off nt
	global_load_dword v103, v[142:143], off nt
	s_load_dwordx2 s[6:7], s[0:1], 0x40
	s_load_dwordx2 s[4:5], s[0:1], 0x88
	s_load_dwordx8 s[20:27], s[0:1], 0x68
	s_movk_i32 s0, 0x188
	v_mul_u32_u24_sdwa v124, v124, s0 dst_sel:DWORD dst_unused:UNUSED_PAD src0_sel:WORD_1 src1_sel:DWORD
	v_add_lshl_u32 v124, v124, v130, 1
	v_lshl_add_u64 v[152:153], s[10:11], 0, v[2:3]
	v_lshrrev_b32_e32 v2, 1, v0
	s_waitcnt vmcnt(29)
	ds_write_b128 v124, v[76:79]
	s_waitcnt vmcnt(28)
	ds_write_b128 v124, v[80:83] offset:25088
	v_mul_u32_u24_sdwa v76, v144, s0 dst_sel:DWORD dst_unused:UNUSED_PAD src0_sel:WORD_1 src1_sel:DWORD
	v_and_b32_e32 v172, 24, v2
	v_add_lshl_u32 v76, v76, v145, 1
	s_bfe_u32 s3, s2, 0x10003
	v_mad_u32_u24 v176, v171, s0, v172
	s_waitcnt vmcnt(27)
	ds_write_b128 v76, v[84:87]
	s_waitcnt vmcnt(26)
	ds_write_b128 v76, v[88:91] offset:25088
	v_mul_u32_u24_sdwa v76, v146, s0 dst_sel:DWORD dst_unused:UNUSED_PAD src0_sel:WORD_1 src1_sel:DWORD
	s_cmp_eq_u32 s3, 0
	s_mulk_i32 s3, 0x180
	v_lshlrev_b32_e32 v175, 1, v176
	v_mov_b32_e32 v127, v3
	v_mov_b32_e32 v129, v3
	v_add_lshl_u32 v76, v76, v147, 1
	v_add_u32_e32 v2, s3, v175
	s_waitcnt vmcnt(25)
	ds_write_b128 v76, v[92:95]
	s_waitcnt vmcnt(24)
	ds_write_b128 v76, v[96:99] offset:25088
	s_waitcnt lgkmcnt(0)
	s_barrier
	v_lshl_add_u64 v[154:155], s[10:11], 0, v[126:127]
	v_lshl_add_u64 v[156:157], s[10:11], 0, v[128:129]
	ds_read_b128 v[76:79], v2
	ds_read_b128 v[80:83], v2 offset:64
	ds_read_b128 v[84:87], v2 offset:12544
	ds_read_b128 v[88:91], v2 offset:12608
	ds_read_b128 v[92:95], v2 offset:128
	ds_read_b128 v[96:99], v2 offset:192
	ds_read_b128 v[126:129], v2 offset:12672
	ds_read_b128 v[132:135], v2 offset:12736
	ds_read_b128 v[136:139], v2 offset:256
	ds_read_b128 v[140:143], v2 offset:320
	ds_read_b128 v[144:147], v2 offset:12800
	ds_read_b128 v[148:151], v2 offset:12864
	s_mov_b32 s1, 0
	s_cselect_b32 s0, 0x1800, 0
	v_lshl_add_u64 v[160:161], v[152:153], 0, s[0:1]
	v_lshl_add_u64 v[156:157], v[156:157], 0, s[0:1]
	v_lshl_add_u64 v[186:187], v[154:155], 0, s[0:1]
	s_setprio 1
	s_waitcnt lgkmcnt(11)
	v_mfma_f32_16x16x32_bf16 v[152:155], v[76:79], v[64:67], 0
	s_waitcnt lgkmcnt(9)
	v_mfma_f32_16x16x32_bf16 v[64:67], v[84:87], v[64:67], 0
	v_mfma_f32_16x16x32_bf16 v[166:169], v[76:79], v[68:71], 0
	v_mfma_f32_16x16x32_bf16 v[68:71], v[84:87], v[68:71], 0
	v_mfma_f32_16x16x32_bf16 v[76:79], v[76:79], v[72:75], 0
	v_mfma_f32_16x16x32_bf16 v[72:75], v[84:87], v[72:75], 0
	s_setprio 0
	global_load_dwordx4 v[84:87], v[160:161], off
	global_load_dwordx4 v[178:181], v[186:187], off
	global_load_dwordx4 v[182:185], v[156:157], off
	s_setprio 1
	v_mfma_f32_16x16x32_bf16 v[152:155], v[80:83], v[52:55], v[152:155]
	s_waitcnt lgkmcnt(8)
	v_mfma_f32_16x16x32_bf16 v[52:55], v[88:91], v[52:55], v[64:67]
	v_mfma_f32_16x16x32_bf16 v[64:67], v[80:83], v[56:59], v[166:169]
	v_mfma_f32_16x16x32_bf16 v[56:59], v[88:91], v[56:59], v[68:71]
	v_mfma_f32_16x16x32_bf16 v[68:71], v[80:83], v[60:63], v[76:79]
	v_mfma_f32_16x16x32_bf16 v[60:63], v[88:91], v[60:63], v[72:75]
	s_setprio 0
	s_nop 1
	global_load_dwordx4 v[72:75], v[160:161], off offset:1024
	global_load_dwordx4 v[76:79], v[186:187], off offset:1024
	global_load_dwordx4 v[80:83], v[156:157], off offset:1024
	s_setprio 1
	s_waitcnt lgkmcnt(7)
	v_mfma_f32_16x16x32_bf16 v[88:91], v[92:95], v[40:43], v[152:155]
	s_waitcnt lgkmcnt(5)
	v_mfma_f32_16x16x32_bf16 v[40:43], v[126:129], v[40:43], v[52:55]
	v_mfma_f32_16x16x32_bf16 v[52:55], v[92:95], v[44:47], v[64:67]
	v_mfma_f32_16x16x32_bf16 v[44:47], v[126:129], v[44:47], v[56:59]
	v_mfma_f32_16x16x32_bf16 v[56:59], v[92:95], v[48:51], v[68:71]
	v_mfma_f32_16x16x32_bf16 v[48:51], v[126:129], v[48:51], v[60:63]
	s_setprio 0
	s_nop 1
	global_load_dwordx4 v[60:63], v[160:161], off offset:2048
	global_load_dwordx4 v[64:67], v[186:187], off offset:2048
	global_load_dwordx4 v[68:71], v[156:157], off offset:2048
	s_setprio 1
	v_mfma_f32_16x16x32_bf16 v[88:91], v[96:99], v[16:19], v[88:91]
	s_waitcnt lgkmcnt(4)
	v_mfma_f32_16x16x32_bf16 v[16:19], v[132:135], v[16:19], v[40:43]
	v_mfma_f32_16x16x32_bf16 v[40:43], v[96:99], v[20:23], v[52:55]
	v_mfma_f32_16x16x32_bf16 v[20:23], v[132:135], v[20:23], v[44:47]
	v_mfma_f32_16x16x32_bf16 v[44:47], v[96:99], v[24:27], v[56:59]
	v_mfma_f32_16x16x32_bf16 v[24:27], v[132:135], v[24:27], v[48:51]
	s_setprio 0
	s_nop 1
	global_load_dwordx4 v[48:51], v[160:161], off offset:3072
	global_load_dwordx4 v[52:55], v[186:187], off offset:3072
	global_load_dwordx4 v[56:59], v[156:157], off offset:3072
	s_setprio 1
	s_waitcnt lgkmcnt(3)
	v_mfma_f32_16x16x32_bf16 v[88:91], v[136:139], v[28:31], v[88:91]
	s_waitcnt lgkmcnt(1)
	v_mfma_f32_16x16x32_bf16 v[16:19], v[144:147], v[28:31], v[16:19]
	v_mfma_f32_16x16x32_bf16 v[28:31], v[136:139], v[32:35], v[40:43]
	v_mfma_f32_16x16x32_bf16 v[20:23], v[144:147], v[32:35], v[20:23]
	v_mfma_f32_16x16x32_bf16 v[32:35], v[136:139], v[36:39], v[44:47]
	v_mfma_f32_16x16x32_bf16 v[24:27], v[144:147], v[36:39], v[24:27]
	s_setprio 0
	s_movk_i32 s0, 0x1000
	v_add_co_u32_e32 v92, vcc, s0, v160
	s_nop 1
	v_addc_co_u32_e32 v93, vcc, 0, v161, vcc
	v_add_co_u32_e32 v94, vcc, s0, v186
	s_nop 1
	v_addc_co_u32_e32 v95, vcc, 0, v187, vcc
	v_add_co_u32_e32 v96, vcc, s0, v156
	global_load_dwordx4 v[36:39], v[92:93], off
	global_load_dwordx4 v[40:43], v[94:95], off
	v_addc_co_u32_e32 v97, vcc, 0, v157, vcc
	global_load_dwordx4 v[44:47], v[96:97], off
	s_setprio 1
	v_mfma_f32_16x16x32_bf16 v[88:91], v[140:143], v[4:7], v[88:91]
	s_waitcnt lgkmcnt(0)
	v_mfma_f32_16x16x32_bf16 v[4:7], v[148:151], v[4:7], v[16:19]
	v_mfma_f32_16x16x32_bf16 v[16:19], v[140:143], v[8:11], v[28:31]
	v_mfma_f32_16x16x32_bf16 v[8:11], v[148:151], v[8:11], v[20:23]
	v_mfma_f32_16x16x32_bf16 v[20:23], v[140:143], v[12:15], v[32:35]
	v_mfma_f32_16x16x32_bf16 v[12:15], v[148:151], v[12:15], v[24:27]
	s_setprio 0
	s_nop 1
	global_load_dwordx4 v[24:27], v[92:93], off offset:1024
	global_load_dwordx4 v[28:31], v[94:95], off offset:1024
	global_load_dwordx4 v[32:35], v[96:97], off offset:1024
	s_cselect_b32 s3, 0x180, 0
	v_add_u32_e32 v2, s3, v175
	ds_read_b128 v[92:95], v2
	ds_read_b128 v[96:99], v2 offset:64
	ds_read_b128 v[126:129], v2 offset:12544
	ds_read_b128 v[132:135], v2 offset:12608
	ds_read_b128 v[136:139], v2 offset:128
	ds_read_b128 v[140:143], v2 offset:192
	ds_read_b128 v[144:147], v2 offset:12672
	ds_read_b128 v[148:151], v2 offset:12736
	ds_read_b128 v[152:155], v2 offset:256
	ds_read_b128 v[166:169], v2 offset:320
	ds_read_b128 v[186:189], v2 offset:12800
	ds_read_b128 v[190:193], v2 offset:12864
	s_setprio 1
	s_waitcnt vmcnt(17) lgkmcnt(11)
	v_mfma_f32_16x16x32_bf16 v[88:91], v[92:95], v[84:87], v[88:91]
	s_waitcnt lgkmcnt(9)
	v_mfma_f32_16x16x32_bf16 v[4:7], v[126:129], v[84:87], v[4:7]
	s_waitcnt vmcnt(16)
	v_mfma_f32_16x16x32_bf16 v[16:19], v[92:95], v[178:181], v[16:19]
	v_mfma_f32_16x16x32_bf16 v[8:11], v[126:129], v[178:181], v[8:11]
	s_waitcnt vmcnt(15)
	v_mfma_f32_16x16x32_bf16 v[20:23], v[92:95], v[182:185], v[20:23]
	v_mfma_f32_16x16x32_bf16 v[12:15], v[126:129], v[182:185], v[12:15]
	s_setprio 0
	s_setprio 1
	s_waitcnt vmcnt(14)
	v_mfma_f32_16x16x32_bf16 v[84:87], v[96:99], v[72:75], v[88:91]
	s_waitcnt lgkmcnt(8)
	v_mfma_f32_16x16x32_bf16 v[4:7], v[132:135], v[72:75], v[4:7]
	s_waitcnt vmcnt(13)
	v_mfma_f32_16x16x32_bf16 v[16:19], v[96:99], v[76:79], v[16:19]
	v_mfma_f32_16x16x32_bf16 v[8:11], v[132:135], v[76:79], v[8:11]
	s_waitcnt vmcnt(12)
	v_mfma_f32_16x16x32_bf16 v[20:23], v[96:99], v[80:83], v[20:23]
	v_mfma_f32_16x16x32_bf16 v[12:15], v[132:135], v[80:83], v[12:15]
	s_setprio 0
	s_setprio 1
	s_waitcnt vmcnt(11) lgkmcnt(7)
	v_mfma_f32_16x16x32_bf16 v[72:75], v[136:139], v[60:63], v[84:87]
	s_waitcnt lgkmcnt(5)
	v_mfma_f32_16x16x32_bf16 v[4:7], v[144:147], v[60:63], v[4:7]
	s_waitcnt vmcnt(10)
	v_mfma_f32_16x16x32_bf16 v[16:19], v[136:139], v[64:67], v[16:19]
	v_mfma_f32_16x16x32_bf16 v[8:11], v[144:147], v[64:67], v[8:11]
	s_waitcnt vmcnt(9)
	v_mfma_f32_16x16x32_bf16 v[20:23], v[136:139], v[68:71], v[20:23]
	v_mfma_f32_16x16x32_bf16 v[12:15], v[144:147], v[68:71], v[12:15]
	s_setprio 0
	s_setprio 1
	s_waitcnt vmcnt(8)
	v_mfma_f32_16x16x32_bf16 v[60:63], v[140:143], v[48:51], v[72:75]
	s_waitcnt lgkmcnt(4)
	v_mfma_f32_16x16x32_bf16 v[4:7], v[148:151], v[48:51], v[4:7]
	s_waitcnt vmcnt(7)
	v_mfma_f32_16x16x32_bf16 v[16:19], v[140:143], v[52:55], v[16:19]
	v_mfma_f32_16x16x32_bf16 v[8:11], v[148:151], v[52:55], v[8:11]
	s_waitcnt vmcnt(6)
	v_mfma_f32_16x16x32_bf16 v[20:23], v[140:143], v[56:59], v[20:23]
	v_mfma_f32_16x16x32_bf16 v[12:15], v[148:151], v[56:59], v[12:15]
	s_setprio 0
	s_setprio 1
	s_waitcnt vmcnt(5) lgkmcnt(3)
	v_mfma_f32_16x16x32_bf16 v[48:51], v[152:155], v[36:39], v[60:63]
	s_waitcnt lgkmcnt(1)
	v_mfma_f32_16x16x32_bf16 v[4:7], v[186:189], v[36:39], v[4:7]
	s_waitcnt vmcnt(4)
	v_mfma_f32_16x16x32_bf16 v[16:19], v[152:155], v[40:43], v[16:19]
	v_mfma_f32_16x16x32_bf16 v[8:11], v[186:189], v[40:43], v[8:11]
	s_waitcnt vmcnt(3)
	v_mfma_f32_16x16x32_bf16 v[20:23], v[152:155], v[44:47], v[20:23]
	v_mfma_f32_16x16x32_bf16 v[12:15], v[186:189], v[44:47], v[12:15]
	s_setprio 0
	s_setprio 1
	s_waitcnt vmcnt(2)
	v_mfma_f32_16x16x32_bf16 v[74:77], v[166:169], v[24:27], v[48:51]
	s_waitcnt lgkmcnt(0)
	v_mfma_f32_16x16x32_bf16 v[90:93], v[190:193], v[24:27], v[4:7]
	s_waitcnt vmcnt(1)
	v_mfma_f32_16x16x32_bf16 v[70:73], v[166:169], v[28:31], v[16:19]
	v_mfma_f32_16x16x32_bf16 v[86:89], v[190:193], v[28:31], v[8:11]
	s_waitcnt vmcnt(0)
	v_mfma_f32_16x16x32_bf16 v[82:85], v[166:169], v[32:35], v[20:23]
	v_mfma_f32_16x16x32_bf16 v[78:81], v[190:193], v[32:35], v[12:15]
	s_setprio 0
	v_or_b32_e32 v124, v163, v171
	v_lshlrev_b32_e32 v2, 2, v124
	global_load_dword v5, v2, s[14:15]
	v_or_b32_e32 v174, 1, v165
	s_movk_i32 s3, 0x310
	v_mov_b32_e32 v4, 0x2df0
	v_lshl_or_b32 v128, v159, 4, v171
	v_lshl_or_b32 v126, v162, 4, v171
	v_mad_u32_u24 v164, v174, s3, v4
	v_lshlrev_b32_e32 v4, 2, v128
	global_load_dword v135, v4, s[14:15]
	v_lshlrev_b32_e32 v2, 2, v126
	global_load_dword v97, v2, s[14:15]
	s_bfe_u32 s10, s2, 0x20003
	s_mul_i32 s11, s10, 0xc00
	s_lshl_b32 s8, s11, 1
	v_mul_u32_u24_e32 v136, 0x1200, v158
	s_add_u32 s8, s12, s8
	v_or_b32_e32 v8, v136, v131
	s_addc_u32 s9, s13, 0
	v_mov_b32_e32 v96, 0xc400
	v_mov_b32_e32 v2, 0x620
	v_lshlrev_b32_e32 v130, 3, v8
	s_add_u32 s14, s8, 0x1000
	s_movk_i32 s2, 0xc40
	v_mov_b32_e32 v6, 0x3100
	v_mov_b32_e32 v7, 0x3410
	v_lshl_or_b32 v95, v124, 1, v96
	v_mad_u32_u24 v166, v174, s3, v2
	v_lshlrev_b32_e32 v2, 4, v8
	v_add_u32_e32 v154, 0x3000, v130
	v_add_u32_e32 v156, 0x6000, v130
	s_addc_u32 s15, s9, 0
	v_mad_u32_u24 v167, v174, s3, s3
	v_mad_u32_u24 v163, v174, s3, v6
	v_mad_u32_u24 v160, v174, s3, v7
	v_mad_u32_u24 v98, v170, s2, v95
	v_lshlrev_b32_e32 v4, 1, v154
	v_lshlrev_b32_e32 v94, 1, v156
	global_load_dwordx4 v[62:65], v2, s[8:9]
	global_load_dwordx4 v[42:45], v2, s[8:9] offset:1024
	global_load_dwordx4 v[58:61], v4, s[8:9]
	global_load_dwordx4 v[38:41], v4, s[8:9] offset:1024
	global_load_dwordx4 v[54:57], v94, s[8:9]
	global_load_dwordx4 v[34:37], v94, s[8:9] offset:1024
	global_load_dwordx4 v[30:33], v2, s[8:9] offset:2048
	global_load_dwordx4 v[14:17], v2, s[8:9] offset:3072
	global_load_dwordx4 v[26:29], v4, s[8:9] offset:2048
	global_load_dwordx4 v[10:13], v4, s[8:9] offset:3072
	global_load_dwordx4 v[22:25], v94, s[8:9] offset:2048
	global_load_dwordx4 v[6:9], v94, s[8:9] offset:3072
	s_add_u32 s8, s8, 0x1400
	v_mad_u32_u24 v99, v174, s3, v95
	v_add_u32_e32 v127, v95, v167
	v_add_u32_e32 v129, v95, v166
	v_add_u32_e32 v132, v95, v164
	v_add_u32_e32 v133, v95, v163
	v_add_u32_e32 v134, v95, v160
	s_addc_u32 s9, s9, 0
	global_load_dwordx4 v[50:53], v2, s[14:15]
	global_load_dwordx4 v[18:21], v2, s[8:9]
	global_load_dwordx4 v[66:69], v4, s[14:15]
	global_load_dwordx4 v[46:49], v4, s[8:9]
	v_mov_b32_e32 v155, v3
	v_mov_b32_e32 v157, v3
	v_mul_u32_u24_e32 v169, 0xc40, v170
	v_mul_u32_u24_e32 v168, 0x310, v174
	s_waitcnt vmcnt(18)
	v_add_f32_e32 v74, v5, v74
	v_add_f32_e32 v75, v5, v75
	v_add_f32_e32 v76, v5, v76
	v_add_f32_e32 v77, v5, v77
	v_add_f32_e32 v90, v5, v90
	v_add_f32_e32 v91, v5, v91
	v_add_f32_e32 v92, v5, v92
	v_cvt_pk_bf16_f32 v74, v74, s0
	v_cvt_pk_bf16_f32 v75, v75, s0
	v_cvt_pk_bf16_f32 v76, v76, s0
	v_cvt_pk_bf16_f32 v77, v77, s0
	v_cvt_pk_bf16_f32 v90, v90, s0
	v_cvt_pk_bf16_f32 v91, v91, s0
	v_cvt_pk_bf16_f32 v92, v92, s0
	ds_write_b16 v98, v74
	ds_write_b16 v99, v75
	ds_write_b16 v127, v76
	ds_write_b16 v129, v77
	ds_write_b16 v132, v90
	ds_write_b16 v133, v91
	ds_write_b16 v134, v92
	v_mov_b32_e32 v74, 0x3720
	v_add_f32_e32 v5, v5, v93
	v_mad_u32_u24 v161, v174, s3, v74
	v_cvt_pk_bf16_f32 v5, v5, s0
	v_add_u32_e32 v74, v95, v161
	ds_write_b16 v74, v5
	v_lshl_add_u32 v90, v126, 1, v96
	s_waitcnt vmcnt(16)
	v_add_f32_e32 v5, v97, v70
	v_cvt_pk_bf16_f32 v5, v5, s0
	v_mad_u32_u24 v70, v170, s2, v90
	ds_write_b16 v70, v5
	v_add_f32_e32 v5, v97, v71
	v_cvt_pk_bf16_f32 v5, v5, s0
	v_mad_u32_u24 v70, v174, s3, v90
	ds_write_b16 v70, v5
	v_add_f32_e32 v5, v97, v72
	v_cvt_pk_bf16_f32 v5, v5, s0
	v_add_u32_e32 v70, v90, v167
	ds_write_b16 v70, v5
	v_add_f32_e32 v5, v97, v73
	v_cvt_pk_bf16_f32 v5, v5, s0
	v_add_u32_e32 v70, v90, v166
	ds_write_b16 v70, v5
	v_add_f32_e32 v5, v97, v86
	v_cvt_pk_bf16_f32 v5, v5, s0
	v_add_u32_e32 v70, v90, v164
	ds_write_b16 v70, v5
	v_add_f32_e32 v5, v97, v87
	v_cvt_pk_bf16_f32 v5, v5, s0
	v_add_u32_e32 v70, v90, v163
	ds_write_b16 v70, v5
	global_load_dwordx4 v[74:77], v94, s[14:15]
	global_load_dwordx4 v[70:73], v94, s[8:9]
	v_add_f32_e32 v5, v97, v88
	v_cvt_pk_bf16_f32 v5, v5, s0
	v_add_u32_e32 v86, v90, v160
	ds_write_b16 v86, v5
	v_add_f32_e32 v86, v97, v89
	v_cvt_pk_bf16_f32 v86, v86, s0
	v_add_u32_e32 v87, v90, v161
	ds_write_b16 v87, v86
	v_lshl_add_u32 v86, v128, 1, v96
	v_add_f32_e32 v82, v135, v82
	v_cvt_pk_bf16_f32 v82, v82, s0
	v_mad_u32_u24 v87, v170, s2, v86
	ds_write_b16 v87, v82
	v_add_f32_e32 v82, v135, v83
	v_cvt_pk_bf16_f32 v82, v82, s0
	v_mad_u32_u24 v83, v174, s3, v86
	ds_write_b16 v83, v82
	v_add_f32_e32 v82, v135, v84
	v_cvt_pk_bf16_f32 v82, v82, s0
	v_add_u32_e32 v83, v86, v167
	ds_write_b16 v83, v82
	v_add_f32_e32 v82, v135, v85
	v_cvt_pk_bf16_f32 v82, v82, s0
	v_add_u32_e32 v83, v86, v166
	v_add_f32_e32 v78, v135, v78
	ds_write_b16 v83, v82
	v_cvt_pk_bf16_f32 v78, v78, s0
	v_add_u32_e32 v82, v86, v164
	ds_write_b16 v82, v78
	v_add_f32_e32 v78, v135, v79
	v_cvt_pk_bf16_f32 v78, v78, s0
	v_add_u32_e32 v79, v86, v163
	ds_write_b16 v79, v78
	v_add_f32_e32 v78, v135, v80
	v_cvt_pk_bf16_f32 v78, v78, s0
	v_add_u32_e32 v79, v86, v160
	ds_write_b16 v79, v78
	v_add_f32_e32 v78, v135, v81
	v_mov_b32_e32 v5, v3
	v_mov_b32_e32 v95, v3
	v_cvt_pk_bf16_f32 v78, v78, s0
	v_add_u32_e32 v79, v86, v161
	v_mov_b32_e32 v127, v3
	v_mov_b32_e32 v129, v3
	ds_write_b16 v79, v78
	v_lshl_add_u64 v[98:99], s[12:13], 0, v[2:3]
	v_lshl_add_u64 v[132:133], s[12:13], 0, v[4:5]
	v_lshl_add_u64 v[134:135], s[12:13], 0, v[94:95]
	s_movk_i32 s2, 0x5f00
	v_mov_b32_e32 v2, v3
	v_mov_b32_e32 v4, v3
	v_mov_b32_e32 v78, v3
	v_mov_b32_e32 v79, v3
	v_mov_b32_e32 v80, v3
	v_mov_b32_e32 v81, v3
	v_mov_b32_e32 v82, v3
	v_mov_b32_e32 v83, v3
	v_mov_b32_e32 v84, v3
	v_mov_b32_e32 v85, v3
	v_mov_b32_e32 v86, v3
	v_mov_b32_e32 v87, v3
	v_mov_b32_e32 v88, v3
	v_mov_b32_e32 v89, v3
	v_mov_b32_e32 v90, v3
	v_mov_b32_e32 v91, v3
	v_mov_b32_e32 v92, v3
	v_mov_b32_e32 v93, v3
	v_mov_b32_e32 v94, v3
	v_mov_b32_e32 v96, v3
	v_mov_b32_e32 v97, v3
	s_waitcnt lgkmcnt(0)
	s_barrier
